# attention tile loop: drop the compiler's vmcnt(0) before the first QK MFMA (K/V tiles stay two ahead); scan pass 1: unit-top wait no longer drains the previous unit's stores
# speedup vs baseline: 1.0041x; 1.0036x over previous
; #define LAS __attribute__((address_space(3)))
; __device__ __forceinline__ void scan_unit(Frame& F, const Args& a, int l, int c, int cn, int h, ScanPref& pf, const bf16x8 (&bfr)[4][4], int par) {
;     ...
;     asm volatile("s_waitcnt vmcnt(" SC1_VM ")" : "+v"(pf.x[0]), "+v"(pf.x[1]), "+v"(pf.x[2]), "+v"(pf.x[3]), "+v"(pf.x[4]) :: "memory");
;     const int chl = 16 * w + l15, ch = 128 * h + chl;
;     ...
;     const f32x4 prm0 = ((const LAS f32x4*)(F.lds + SC_PRM))[chl], prm1 = ((const LAS f32x4*)(F.lds + SC_PRM))[128 + chl];
;     ...
;     const f32x4* SPT = (const f32x4*)(ws + WS_SPT);
;     const f32x4 prm0 = SPT[((size_t)l * 2 + 0) * D + ch], prm1 = SPT[((size_t)l * 2 + 1) * D + ch];
;     ...
;     {
;         const int ch8 = tid & 15; const int cb = 128 * h + 8 * ch8;
;         const float* cw = (a.in[10] + F.zo) + (size_t)l * 4 * D + cb; const float* cbp = (a.in[11] + F.zo) + l * D + cb;
;         f32x4 w4[4][2];
;     ...
;         const LAS float* cwt = (const LAS float*)(F.lds + SC_CW) + 8 * ch8; (void)cw; (void)cbp;
; #pragma unroll
;         for (int j = 0; j < 4; ++j) { w4[j][0] = *(const LAS f32x4*)(cwt + j * 128); w4[j][1] = *(const LAS f32x4*)(cwt + j * 128 + 4); }
;         const f32x4 b0 = *(const LAS f32x4*)(cwt + 4 * 128), b1 = *(const LAS f32x4*)(cwt + 4 * 128 + 4);
;     ...
; #pragma unroll
;         for (int j = 0; j < 4; ++j) { w4[j][0] = *(const f32x4*)(cw + j * D); w4[j][1] = *(const f32x4*)(cw + j * D + 4); }
;         const f32x4 b0 = *(const f32x4*)(cbp), b1 = *(const f32x4*)(cbp + 4);
;     ...
; #pragma unroll
;         for (int i = 0; i < 2; ++i) { const int t = 2 * (tid >> 4) + i, row = sc_rho(t);
;             f32x4 a0 = b0, a1 = b1;
; #pragma unroll
;             for (int j = 0; j < 4; ++j) { const u32x4 xv = pf.x[i + j];
;                 a0[0] += bflo(xv.x) * w4[j][0][0]; a0[1] += bfhi(xv.x) * w4[j][0][1]; a0[2] += bflo(xv.y) * w4[j][0][2]; a0[3] += bfhi(xv.y) * w4[j][0][3];
;                 a1[0] += bflo(xv.z) * w4[j][1][0]; a1[1] += bfhi(xv.z) * w4[j][1][1]; a1[2] += bflo(xv.w) * w4[j][1][2]; a1[3] += bfhi(xv.w) * w4[j][1][3]; }
;             u32x4 o; o.x = pk2(a0[0], a0[1]); o.y = pk2(a0[2], a0[3]); o.z = pk2(a1[0], a1[1]); o.w = pk2(a1[2], a1[3]);
;             *(LAS u32x4*)(lds + SC_X + row * SC_STR + ch8 * 16) = o;
;         }
;     }
;     __syncthreads();
;     if (cn >= 0) scan_prefetch(pf, P, cn, h, tid);
.LBB13_488:
	s_waitcnt vmcnt(8)
	s_waitcnt vmcnt(8)
	global_load_dwordx4 v[90:93], v[162:163], off
	global_load_dwordx4 v[86:89], v[164:165], off
	global_load_dwordx4 v[108:111], v[166:167], off offset:16
	global_load_dwordx4 v[120:123], v[166:167], off
	global_load_dwordx4 v[104:107], v[168:169], off offset:16
	global_load_dwordx4 v[124:127], v[168:169], off
	global_load_dwordx4 v[100:103], v[170:171], off offset:16
	global_load_dwordx4 v[128:131], v[170:171], off
	global_load_dwordx4 v[94:97], v[172:173], off offset:16
	global_load_dwordx4 v[116:119], v[172:173], off
	global_load_dwordx4 v[112:115], v[174:175], off offset:16
	global_load_dwordx4 v[132:135], v[174:175], off
	v_lshlrev_b32_e32 v136, 16, v6
	v_and_b32_e32 v137, 0xffff0000, v6
	v_lshlrev_b32_e32 v140, 16, v2
	v_and_b32_e32 v141, 0xffff0000, v2
	v_lshlrev_b32_e32 v152, 16, v8
	v_and_b32_e32 v153, 0xffff0000, v8
	v_lshlrev_b32_e32 v154, 16, v4
	v_and_b32_e32 v155, 0xffff0000, v4
	v_lshlrev_b32_e32 v142, 16, v10
	v_and_b32_e32 v143, 0xffff0000, v10
	v_lshlrev_b32_e32 v156, 16, v12
	v_and_b32_e32 v157, 0xffff0000, v12
	v_lshlrev_b32_e32 v144, 16, v14
	v_and_b32_e32 v145, 0xffff0000, v14
	v_lshlrev_b32_e32 v158, 16, v16
	v_and_b32_e32 v159, 0xffff0000, v16
	v_lshlrev_b32_e32 v138, 16, v7
	v_and_b32_e32 v139, 0xffff0000, v7
	v_lshlrev_b32_e32 v146, 16, v3
	v_and_b32_e32 v147, 0xffff0000, v3
	v_lshlrev_b32_e32 v180, 16, v9
	v_and_b32_e32 v181, 0xffff0000, v9
	v_lshlrev_b32_e32 v182, 16, v5
	v_and_b32_e32 v183, 0xffff0000, v5
	v_lshlrev_b32_e32 v148, 16, v11
	v_and_b32_e32 v149, 0xffff0000, v11
	v_lshlrev_b32_e32 v184, 16, v13
	v_and_b32_e32 v185, 0xffff0000, v13
	v_lshlrev_b32_e32 v150, 16, v15
	v_and_b32_e32 v151, 0xffff0000, v15
	v_lshlrev_b32_e32 v186, 16, v17
	v_and_b32_e32 v187, 0xffff0000, v17
	s_cmp_lt_i32 s59, 0
	s_cselect_b64 s[36:37], -1, 0
	s_and_b64 vcc, exec, s[36:37]
	s_waitcnt vmcnt(1)
	v_pk_fma_f32 v[152:153], v[108:109], v[152:153], v[112:113]
	s_waitcnt vmcnt(0)
	v_pk_fma_f32 v[136:137], v[120:121], v[136:137], v[132:133]
	v_pk_fma_f32 v[120:121], v[120:121], v[140:141], v[132:133]
	v_pk_fma_f32 v[108:109], v[108:109], v[154:155], v[112:113]
	v_pk_fma_f32 v[136:137], v[124:125], v[140:141], v[136:137]
	v_pk_fma_f32 v[152:153], v[104:105], v[154:155], v[152:153]
	v_pk_fma_f32 v[120:121], v[124:125], v[142:143], v[120:121]
	v_pk_fma_f32 v[104:105], v[104:105], v[156:157], v[108:109]
	v_pk_fma_f32 v[136:137], v[128:129], v[142:143], v[136:137]
	v_pk_fma_f32 v[152:153], v[100:101], v[156:157], v[152:153]
	v_pk_fma_f32 v[120:121], v[128:129], v[144:145], v[120:121]
	v_lshlrev_b32_e32 v124, 16, v18
	v_and_b32_e32 v125, 0xffff0000, v18
	v_pk_fma_f32 v[100:101], v[100:101], v[158:159], v[104:105]
	v_lshlrev_b32_e32 v104, 16, v20
	v_and_b32_e32 v105, 0xffff0000, v20
	v_pk_fma_f32 v[136:137], v[116:117], v[144:145], v[136:137]
	v_pk_fma_f32 v[138:139], v[122:123], v[138:139], v[134:135]
	v_pk_fma_f32 v[152:153], v[94:95], v[158:159], v[152:153]
	v_pk_fma_f32 v[180:181], v[110:111], v[180:181], v[114:115]
	v_pk_fma_f32 v[116:117], v[116:117], v[124:125], v[120:121]
	v_pk_fma_f32 v[120:121], v[122:123], v[146:147], v[134:135]
	v_pk_fma_f32 v[100:101], v[94:95], v[104:105], v[100:101]
	v_pk_fma_f32 v[94:95], v[110:111], v[182:183], v[114:115]
	v_pk_fma_f32 v[138:139], v[126:127], v[146:147], v[138:139]
	v_pk_fma_f32 v[180:181], v[106:107], v[182:183], v[180:181]
	v_pk_fma_f32 v[120:121], v[126:127], v[148:149], v[120:121]
	v_pk_fma_f32 v[94:95], v[106:107], v[184:185], v[94:95]
	v_pk_fma_f32 v[138:139], v[130:131], v[148:149], v[138:139]
	v_pk_fma_f32 v[180:181], v[102:103], v[184:185], v[180:181]
	v_pk_fma_f32 v[120:121], v[130:131], v[150:151], v[120:121]
	v_lshlrev_b32_e32 v122, 16, v19
	v_and_b32_e32 v123, 0xffff0000, v19
	v_pk_fma_f32 v[94:95], v[102:103], v[186:187], v[94:95]
	v_lshlrev_b32_e32 v102, 16, v21
	v_and_b32_e32 v103, 0xffff0000, v21
	v_pk_fma_f32 v[138:139], v[118:119], v[150:151], v[138:139]
	v_pk_fma_f32 v[180:181], v[96:97], v[186:187], v[180:181]
	v_pk_fma_f32 v[118:119], v[118:119], v[122:123], v[120:121]
	v_pk_fma_f32 v[102:103], v[96:97], v[102:103], v[94:95]
	v_cvt_pk_bf16_f32 v136, v136, v137
	v_cvt_pk_bf16_f32 v137, v138, v139
	v_cvt_pk_bf16_f32 v138, v152, v153
	v_cvt_pk_bf16_f32 v139, v180, v181
	v_cvt_pk_bf16_f32 v94, v116, v117
	v_cvt_pk_bf16_f32 v95, v118, v119
	v_cvt_pk_bf16_f32 v96, v100, v101
	v_cvt_pk_bf16_f32 v97, v102, v103
	ds_write_b128 v199, v[136:139]
	ds_write_b128 v199, v[94:97] offset:272
	s_waitcnt lgkmcnt(0)
	s_barrier
	s_cbranch_vccnz .LBB13_500
	s_lshl_b32 s8, s59, 6
	s_and_b32 s9, s8, 0x2000
	s_and_b32 s44, s8, 0xffffff00
	s_add_i32 s43, s9, 0x2000
	s_add_i32 s45, s44, 0x100
	s_cmpk_lt_u32 s59, 0x100
	v_add_u32_e32 v18, s8, v195
	s_cselect_b32 s43, s43, s45
	s_cselect_b32 s44, s9, s44
	v_add_u32_e32 v10, -2, v18
	v_mov_b32_e32 v4, v98
	v_mov_b32_e32 v5, v98
	v_cmp_le_i32_e32 vcc, s44, v10
	v_cmp_gt_i32_e64 s[8:9], s43, v10
	v_mov_b32_e32 v2, v98
	v_mov_b32_e32 v3, v98
	v_mov_b64_e32 v[8:9], v[4:5]
	s_and_b64 s[60:61], vcc, s[8:9]
	v_mov_b64_e32 v[6:7], v[2:3]
	s_and_saveexec_b64 s[8:9], s[60:61]
	s_cbranch_execz .LBB13_491
	v_mad_u64_u32 v[6:7], s[60:61], v10, s91, v[178:179]
	global_load_dwordx4 v[6:9], v[6:7], off offset:3072

; #define LAS __attribute__((address_space(3)))
; #define A3_SB() do { if (!A3_NOSBAR) __builtin_amdgcn_sched_barrier(0); } while (0)
; #define A3_BAR() do { asm volatile("s_waitcnt lgkmcnt(0)" ::: "memory"); __builtin_amdgcn_s_barrier(); asm volatile("" ::: "memory"); } while (0)
; #define A3_BAR() do { asm volatile("s_waitcnt lgkmcnt(0)" ::: "memory"); __builtin_amdgcn_s_barrier(); asm volatile("" ::: "memory"); } while (0)
; __device__ __forceinline__ void a3_qk(f32x16& p, const LAS unsigned char* Kh, const bf16x8 (&qr)[8], int base) {
; #pragma unroll
;     for (int r = 0; r < 16; ++r) p[r] = 0.f;
; #pragma unroll
;     for (int d0 = 0; d0 < 8; ++d0) { const bf16x8 b = *(const LAS bf16x8*)(Kh + (base ^ (32 * d0))); if (A3_PRIO) __builtin_amdgcn_s_setprio(1); p = __builtin_amdgcn_mfma_f32_32x32x16_bf16(b, qr[d0], p, 0, 0, 0); if (A3_PRIO) __builtin_amdgcn_s_setprio(0); }
; }
; __device__ __forceinline__ void attn_stream(Frame& F, const float* sinkl, int u_first, int u_stride, int n_lat, int u_extra) {
;     ...
;         for (int j = 1; j < NT; ++j) {
;             if (j + 1 < NT || has_next) asm volatile("s_waitcnt vmcnt(4)" ::: "memory"); else asm volatile("s_waitcnt vmcnt(0)" ::: "memory");
;             A3_BAR();
;             const int bc = ((rb + j) & 3) * A3_BUF, bp = ((rb + j - 1) & 3) * A3_BUF;
;             A3_SB(); a3_qk(pE, lds + bc + A3_K, qr, kbase);
;             a3_fsm(pO, alO, l_reg, pf); A3_SB();
;             if (j + 2 < NT) A3S_DMA(cu, j + 2, rb + j + 2); else if (has_next) A3S_DMA(nx, j + 2 - NT, rb + j + 2);
.LBB13_540:
	s_add_i32 s4, s95, 0xfffe8000
	s_and_b32 s43, s4, 0x18000
	s_add_i32 s4, s57, s43
	s_waitcnt lgkmcnt(0)
	s_barrier
	v_add_u32_e32 v90, s4, v151
	ds_read_b128 v[66:69], v90 offset:16384
	s_add_i32 s44, s7, s89
	s_setprio 1
	s_waitcnt lgkmcnt(0)
	v_mfma_f32_32x32x16_bf16 v[66:81], v[66:69], v[100:103], 0
	s_setprio 0
	v_add_u32_e32 v181, s4, v153
	ds_read_b128 v[92:95], v181 offset:16384
	s_setprio 1
	s_waitcnt lgkmcnt(0)
	v_mfma_f32_32x32x16_bf16 v[66:81], v[92:95], v[104:107], v[66:81]
	s_setprio 0
	v_add_u32_e32 v182, s4, v154
	ds_read_b128 v[92:95], v182 offset:16384
	s_setprio 1
	s_waitcnt lgkmcnt(0)
	v_mfma_f32_32x32x16_bf16 v[66:81], v[92:95], v[108:111], v[66:81]
	s_setprio 0
	v_add_u32_e32 v183, s4, v155
	ds_read_b128 v[92:95], v183 offset:16384
	s_setprio 1
	s_waitcnt lgkmcnt(0)
	v_mfma_f32_32x32x16_bf16 v[66:81], v[92:95], v[112:115], v[66:81]
	s_setprio 0
	v_add_u32_e32 v184, s4, v156
	ds_read_b128 v[92:95], v184 offset:16384
	s_setprio 1
	s_waitcnt lgkmcnt(0)
	v_mfma_f32_32x32x16_bf16 v[66:81], v[92:95], v[116:119], v[66:81]
	s_setprio 0
	v_add_u32_e32 v185, s4, v157
	ds_read_b128 v[92:95], v185 offset:16384
	s_setprio 1
	s_waitcnt lgkmcnt(0)
	v_mfma_f32_32x32x16_bf16 v[66:81], v[92:95], v[120:123], v[66:81]
	s_setprio 0
	v_add_u32_e32 v186, s4, v158
	ds_read_b128 v[92:95], v186 offset:16384
	s_setprio 1
	s_waitcnt lgkmcnt(0)
	v_mfma_f32_32x32x16_bf16 v[66:81], v[92:95], v[124:127], v[66:81]
	s_setprio 0
	v_add_u32_e32 v187, s4, v159
	ds_read_b128 v[92:95], v187 offset:16384
	s_setprio 1
	s_waitcnt lgkmcnt(0)
	v_mfma_f32_32x32x16_bf16 v[66:81], v[92:95], v[128:131], v[66:81]
	s_setprio 0
	s_cmp_ge_u32 s89, s87
	s_cbranch_scc0 .LBB13_545
	s_mov_b64 s[40:41], 0
	s_and_b64 vcc, exec, s[28:29]
	s_mov_b64 s[4:5], 0
	s_cbranch_vccz .LBB13_543
	s_add_i32 s4, s44, -4
	s_cmp_lt_i32 s4, s72
	s_cselect_b32 s5, 0, s72
	s_cselect_b32 s45, s86, s76
	s_sub_i32 s46, s4, s5
	s_mov_b64 s[4:5], -1
	s_and_b64 vcc, exec, s[40:41]
	s_mov_b64 s[40:41], s[34:35]
	s_cbranch_vccz .LBB13_546
	s_branch .LBB13_544
